# speedup vs baseline: 1.1514x; 1.0002x over previous
_Z11attn_kernelPKDF16_PDF16_PKfS3_S3_PfS4_ii:
	s_cmpk_lt_u32 s2, 0x200
	s_mov_b64 s[4:5], -1
	s_cbranch_scc0 .LBB2_36
	v_lshrrev_b32_e32 v92, 6, v0
	s_movk_i32 s3, 0x100
	v_cmp_gt_u32_e64 s[6:7], s3, v0
	s_movk_i32 s3, 0xff
	v_lshlrev_b32_e32 v2, 4, v92
	v_lshlrev_b32_e32 v108, 3, v0
	v_cmp_lt_u32_e32 vcc, s3, v0
	v_and_b32_e32 v1, 32, v2
	v_and_b32_e32 v18, 24, v108
	s_movk_i32 s3, 0x400
	v_bfe_u32 v3, v0, 2, 4
	v_or3_b32 v4, v1, v18, s3
	s_and_saveexec_b64 s[4:5], vcc
	s_xor_b64 s[4:5], exec, s[4:5]
	v_lshlrev_b32_e32 v1, 5, v92
	v_and_or_b32 v1, v1, 32, v3
	s_movk_i32 s3, 0x640
	v_mad_u32_u24 v82, v1, s3, v4
	s_or_saveexec_b64 s[4:5], s[4:5]
	v_bfe_u32 v109, v0, 3, 3
	s_xor_b64 exec, exec, s[4:5]
	v_or_b32_e32 v1, v2, v109
	v_lshrrev_b32_e32 v2, 1, v1
	v_xor_b32_e32 v2, v2, v0
	v_mul_u32_u24_e32 v1, 0x640, v1
	v_lshlrev_b32_e32 v2, 3, v2
	v_and_or_b32 v1, v2, 56, v1
	v_add_u32_e32 v82, 0x200, v1
	s_or_b64 exec, exec, s[4:5]
	s_load_dwordx2 s[12:13], s[0:1], 0x0
	v_and_b32_e32 v96, 3, v92
	v_lshl_or_b32 v5, v96, 1, 1
	s_and_saveexec_b64 s[4:5], vcc
	s_xor_b64 s[4:5], exec, s[4:5]
	v_lshlrev_b32_e32 v1, 4, v5
	v_and_or_b32 v1, v1, 48, v3
	s_movk_i32 s3, 0x640
	v_mad_u32_u24 v2, v1, s3, v4
	s_or_saveexec_b64 s[4:5], s[4:5]
	v_and_b32_e32 v94, 63, v0
	s_xor_b64 exec, exec, s[4:5]
	v_lshl_or_b32 v1, v5, 3, v109
	v_lshrrev_b32_e32 v2, 1, v1
	v_xor_b32_e32 v2, v2, v0
	v_mul_u32_u24_e32 v1, 0x640, v1
	v_lshlrev_b32_e32 v2, 3, v2
	v_and_or_b32 v1, v2, 56, v1
	v_add_u32_e32 v2, 0x200, v1
	s_or_b64 exec, exec, s[4:5]
	v_mov_b32_e32 v1, 0x100
	v_sub_co_u32_e32 v1, vcc, s2, v1
	s_lshr_b32 s3, s2, 6
	v_readfirstlane_b32 s4, v1
	s_sub_i32 s3, 7, s3
	s_lshr_b32 s8, s4, 6
	s_and_b64 s[4:5], vcc, exec
	s_cselect_b32 s4, s3, s8
	v_and_b32_e32 v95, 31, v0
	s_lshl_b32 s18, s4, 7
	s_lshl_b32 s3, s2, 10
	v_lshlrev_b32_e32 v110, 5, v96
	s_and_b32 s19, s3, 0x1c00
	v_or3_b32 v99, v110, v95, s18
	s_lshl_b32 s3, s2, 3
	v_add_u32_e32 v3, s19, v99
	s_and_b32 s3, s3, 0x1c0
	s_lshl_b32 s21, s4, 1
	s_movk_i32 s4, 0xc80
	s_waitcnt lgkmcnt(0)
	v_mov_b64_e32 v[4:5], s[12:13]
	s_mov_b32 s5, 0
	v_mad_u64_u32 v[4:5], s[8:9], v3, s4, v[4:5]
	s_lshl_b32 s4, s3, 1
	s_mul_i32 s14, s19, 0xc80
	v_lshl_add_u64 v[4:5], v[4:5], 0, s[4:5]
	s_add_u32 s5, s12, s14
	s_addc_u32 s8, s13, 0
	s_add_u32 s4, s5, s4
	s_addc_u32 s5, s8, 0
	v_lshlrev_b32_e32 v34, 11, v92
	s_cmp_lg_u32 0, -1
	v_mov_b32_e32 v83, 0
	v_readfirstlane_b32 s8, v34
	s_cselect_b32 s9, 0, 0
	v_lshlrev_b64 v[84:85], 1, v[82:83]
	s_add_i32 s8, s8, s9
	v_lshl_add_u64 v[6:7], s[4:5], 0, v[84:85]
	s_mov_b32 s9, m0
	s_mov_b32 m0, s8
	s_nop 0
	global_load_lds_dwordx4 v[6:7], off
	s_mov_b32 m0, s9
	v_mov_b32_e32 v3, v83
	v_lshlrev_b64 v[86:87], 1, v[2:3]
	s_add_i32 s9, s8, 0x400
	v_lshl_add_u64 v[2:3], s[4:5], 0, v[86:87]
	s_mov_b32 s10, m0
	s_mov_b32 m0, s9
	s_nop 0
	global_load_lds_dwordx4 v[2:3], off
	s_mov_b32 m0, s10
	s_add_i32 s9, s8, 0x4000
	s_add_u32 s4, s4, 0x32000
	s_addc_u32 s5, s5, 0
	v_lshrrev_b32_e32 v93, 5, v94
	v_lshl_add_u64 v[2:3], s[4:5], 0, v[84:85]
	s_mov_b32 s10, m0
	s_mov_b32 m0, s9
	s_nop 0
	global_load_lds_dwordx4 v[2:3], off
	s_mov_b32 m0, s10
	v_lshl_add_u64 v[2:3], s[4:5], 0, v[86:87]
	v_lshlrev_b32_e32 v82, 4, v93
	s_addk_i32 s8, 0x4400
	s_mov_b32 s4, m0
	s_mov_b32 m0, s8
	s_nop 0
	global_load_lds_dwordx4 v[2:3], off
	s_mov_b32 m0, s4
	v_lshl_add_u64 v[2:3], v[4:5], 0, v[82:83]
	global_load_dwordx4 v[78:81], v[2:3], off
	global_load_dwordx4 v[74:77], v[2:3], off offset:32
	global_load_dwordx4 v[70:73], v[2:3], off offset:64
	global_load_dwordx4 v[66:69], v[2:3], off offset:96
	s_load_dwordx2 s[8:9], s[0:1], 0x8
	v_lshrrev_b32_e32 v2, 1, v0
	v_bfe_u32 v3, v0, 1, 3
	v_lshlrev_b32_e32 v4, 4, v0
	v_lshlrev_b32_e32 v5, 1, v0
	v_lshlrev_b32_e32 v19, 7, v95
	v_bitop3_b32 v20, v93, v2, 7 bitop3:0x78
	v_bitop3_b32 v21, v93, v3, 2 bitop3:0x36
	v_bitop3_b32 v22, v93, v3, 4 bitop3:0x36
	v_bitop3_b32 v23, v93, v3, 6 bitop3:0x36
	v_and_b32_e32 v24, 0xc0, v4
	v_and_b32_e32 v25, 32, v5
	v_mov_b32_e32 v16, v83
	v_mov_b32_e32 v17, v83
	v_lshl_or_b32 v106, v20, 4, v19
	v_lshl_or_b32 v105, v21, 4, v19
	v_lshl_or_b32 v104, v22, 4, v19
	v_lshl_or_b32 v103, v23, 4, v19
	v_lshl_or_b32 v19, v93, 8, v24
	v_lshrrev_b32_e32 v97, 8, v0
	v_mov_b32_e32 v2, v83
	v_mov_b32_e32 v3, v83
	v_mov_b32_e32 v4, v83
	v_mov_b32_e32 v5, v83
	v_mov_b32_e32 v6, v83
	v_mov_b32_e32 v7, v83
	v_mov_b32_e32 v8, v83
	v_mov_b32_e32 v9, v83
	v_mov_b32_e32 v10, v83
	v_mov_b32_e32 v11, v83
	v_mov_b32_e32 v12, v83
	v_mov_b32_e32 v13, v83
	v_mov_b32_e32 v14, v83
	v_mov_b32_e32 v15, v83
	v_or3_b32 v98, v19, v25, v18
	s_add_i32 s20, 0, 0x10000
	v_mov_b64_e32 v[32:33], v[16:17]
	v_cmp_gt_u32_e32 vcc, s21, v97
	v_lshl_add_u32 v100, v92, 7, s20
	v_mov_b32_e32 v102, 0xff800000
	v_mbcnt_lo_u32_b32 v101, -1, 0
	v_mov_b32_e32 v107, v97
	v_mov_b64_e32 v[30:31], v[14:15]
	v_mov_b64_e32 v[28:29], v[12:13]
	v_mov_b64_e32 v[26:27], v[10:11]
	v_mov_b64_e32 v[24:25], v[8:9]
	v_mov_b64_e32 v[22:23], v[6:7]
	v_mov_b64_e32 v[20:21], v[4:5]
	v_mov_b64_e32 v[18:19], v[2:3]
	s_waitcnt vmcnt(3)
	s_waitcnt vmcnt(2)
	s_waitcnt vmcnt(1)
	s_waitcnt vmcnt(0)
	s_and_saveexec_b64 s[10:11], vcc
	s_cbranch_execz .LBB2_18
	s_cmp_lg_u32 0, -1
	s_cselect_b32 s4, 0, 0
	s_lshl_b32 s15, s2, 4
	s_and_b32 s15, s15, 0x380
	s_add_u32 s14, s14, s15
	s_addc_u32 s15, 0, 0
	s_add_u32 s12, s12, s14
	v_mov_b32_e32 v2, 0
	s_addc_u32 s13, s13, s15
	v_mov_b32_e32 v16, v2
	v_mov_b32_e32 v17, v2
	s_add_u32 s12, s12, 0x96000
	v_mov_b32_e32 v3, v2
	v_mov_b32_e32 v4, v2
	v_mov_b32_e32 v5, v2
	v_mov_b32_e32 v6, v2
	v_mov_b32_e32 v7, v2
	v_mov_b32_e32 v8, v2
	v_mov_b32_e32 v9, v2
	v_mov_b32_e32 v10, v2
	v_mov_b32_e32 v11, v2
	v_mov_b32_e32 v12, v2
	v_mov_b32_e32 v13, v2
	v_mov_b32_e32 v14, v2
	v_mov_b32_e32 v15, v2
	v_mov_b64_e32 v[32:33], v[16:17]
	v_add_u32_e32 v108, s4, v34
	v_cmp_gt_u32_e64 s[4:5], 32, v94
	s_addc_u32 s13, s13, 0
	v_lshlrev_b32_e32 v109, 14, v97
	v_mov_b32_e32 v88, 0xff800000
	s_mov_b32 s22, 0xc000
	s_mov_b64 s[14:15], 0
	v_mbcnt_hi_u32_b32 v110, -1, v101
	s_mov_b32 s23, 0x3e38aa3b
	s_mov_b32 s24, 0x41000000
	v_add_u32_e32 v111, v100, v82
	s_mov_b32 s25, 0xff800000
	v_bfrev_b32_e32 v112, 1
	v_mov_b32_e32 v107, v97
	v_mov_b64_e32 v[30:31], v[14:15]
	v_mov_b64_e32 v[28:29], v[12:13]
	v_mov_b64_e32 v[26:27], v[10:11]
	v_mov_b64_e32 v[24:25], v[8:9]
	v_mov_b64_e32 v[22:23], v[6:7]
	v_mov_b64_e32 v[20:21], v[4:5]
	v_mov_b64_e32 v[18:19], v[2:3]
	v_mov_b32_e32 v113, v2
	v_readfirstlane_b32 s28, v97
	s_nop 3
	s_cmp_eq_u32 s28, 1
	s_cbranch_scc0 .Lprio_skip
	s_setprio 1
.Lprio_skip:
	s_branch .LBB2_13
.LBB2_11:
	s_or_b64 exec, exec, s[16:17]
	s_waitcnt lgkmcnt(0)
	ds_read_b128 v[116:119], v111
	ds_read_b128 v[120:123], v111 offset:32
	ds_read_b128 v[124:127], v111 offset:64
	ds_read_b128 v[88:91], v111 offset:96
	v_mul_f32_e32 v113, v113, v82
	s_waitcnt lgkmcnt(3)
	v_pk_mul_f32 v[20:21], v[20:21], v[118:119]
	s_waitcnt lgkmcnt(2)
	v_pk_mul_f32 v[22:23], v[22:23], v[120:121]
	s_waitcnt lgkmcnt(1)
	v_pk_mul_f32 v[26:27], v[26:27], v[124:125]
	s_waitcnt lgkmcnt(0)
	v_pk_mul_f32 v[30:31], v[30:31], v[88:89]
	v_pk_mul_f32 v[32:33], v[32:33], v[90:91]
	v_pk_mul_f32 v[28:29], v[28:29], v[126:127]
	v_pk_mul_f32 v[24:25], v[24:25], v[122:123]
	v_pk_mul_f32 v[18:19], v[18:19], v[116:117]
	v_pk_mul_f32 v[14:15], v[14:15], v[88:89]
	v_pk_mul_f32 v[10:11], v[10:11], v[124:125]
	v_pk_mul_f32 v[6:7], v[6:7], v[120:121]
	v_pk_mul_f32 v[16:17], v[16:17], v[90:91]
	v_pk_mul_f32 v[12:13], v[12:13], v[126:127]
	v_pk_mul_f32 v[8:9], v[8:9], v[122:123]
	v_pk_mul_f32 v[4:5], v[4:5], v[118:119]
	v_pk_mul_f32 v[2:3], v[2:3], v[116:117]

	.amdhsa_kernel _Z11attn_kernelPKDF16_PDF16_PKfS3_S3_PfS4_ii
		.amdhsa_group_segment_fixed_size 0
		.amdhsa_private_segment_fixed_size 0
		.amdhsa_kernarg_size 64
		.amdhsa_user_sgpr_count 2
		.amdhsa_user_sgpr_dispatch_ptr 0
		.amdhsa_user_sgpr_queue_ptr 0
		.amdhsa_user_sgpr_kernarg_segment_ptr 1
		.amdhsa_user_sgpr_dispatch_id 0
		.amdhsa_user_sgpr_kernarg_preload_length 0
		.amdhsa_user_sgpr_kernarg_preload_offset 0
		.amdhsa_user_sgpr_private_segment_size 0
		.amdhsa_uses_dynamic_stack 0
		.amdhsa_enable_private_segment 0
		.amdhsa_system_sgpr_workgroup_id_x 1
		.amdhsa_system_sgpr_workgroup_id_y 0
		.amdhsa_system_sgpr_workgroup_id_z 0
		.amdhsa_system_sgpr_workgroup_info 0
		.amdhsa_system_vgpr_workitem_id 0
		.amdhsa_next_free_vgpr 128
		.amdhsa_next_free_sgpr 30
		.amdhsa_accum_offset 128
		.amdhsa_reserve_vcc 1
		.amdhsa_float_round_mode_32 0
		.amdhsa_float_round_mode_16_64 0
		.amdhsa_float_denorm_mode_32 3
		.amdhsa_float_denorm_mode_16_64 3
		.amdhsa_dx10_clamp 1
		.amdhsa_ieee_mode 1
		.amdhsa_fp16_overflow 0
		.amdhsa_tg_split 0
		.amdhsa_exception_fp_ieee_invalid_op 0
		.amdhsa_exception_fp_denorm_src 0
		.amdhsa_exception_fp_ieee_div_zero 0
		.amdhsa_exception_fp_ieee_overflow 0
		.amdhsa_exception_fp_ieee_underflow 0
		.amdhsa_exception_fp_ieee_inexact 0
		.amdhsa_exception_int_div_zero 0
	.end_amdhsa_kernel
